# NA main loop: bias/mask/max/exp/row-sum/pack of the 12 scores per lane that the 16-column window always masks (which 12 depends only on wave parity) skipped via a wave-uniform branch; P registers zero
# speedup vs baseline: 1.0031x; 1.0031x over previous
.LBB0_469:
	v_lshl_add_u64 v[66:67], v[154:155], 0, s[96:97]
	v_add_co_u32_e32 v70, vcc, 0x52002000, v66
	v_lshl_add_u64 v[68:69], v[156:157], 0, s[96:97]
	s_nop 0
	v_addc_co_u32_e32 v71, vcc, 0, v67, vcc
	global_load_dwordx2 v[164:165], v[70:71], off
	v_add_co_u32_e32 v70, vcc, 0x52002000, v68
	s_and_b32 s1, s3, 0x4000
	s_nop 0
	v_addc_co_u32_e32 v71, vcc, 0, v69, vcc
	v_add_co_u32_e32 v66, vcc, 0x4e002000, v66
	global_load_dwordx2 v[162:163], v[70:71], off
	s_nop 0
	v_addc_co_u32_e32 v67, vcc, 0, v67, vcc
	global_load_dwordx2 v[160:161], v[66:67], off
	v_add_co_u32_e32 v66, vcc, 0x4e002000, v68
	s_add_i32 s72, s1, 0
	s_nop 0
	v_addc_co_u32_e32 v67, vcc, 0, v69, vcc
	v_add3_u32 v0, s72, v199, v189
	v_add3_u32 v98, s72, v197, v189
	global_load_dwordx2 v[158:159], v[66:67], off
	s_cmp_lt_u32 s92, s84
	s_cbranch_scc1 .Lna_skip
	s_cmp_ge_u32 s92, s88
	s_cbranch_scc1 .Lna_skip
	v_add_u32_e32 v0, s72, v189
	v_add_u32_e32 v66, v0, v199
	ds_read_b128 v[66:69], v66 offset:32768
	v_add_u32_e32 v70, v0, v199
	ds_read_b128 v[70:73], v70 offset:40960
	v_add_u32_e32 v98, v0, v197
	ds_read_b128 v[98:101], v98 offset:32768
	v_add_u32_e32 v102, v0, v197
	ds_read_b128 v[102:105], v102 offset:40960
	v_add_u32_e32 v106, v0, v195
	ds_read_b128 v[106:109], v106 offset:32768
	v_add_u32_e32 v110, v0, v195
	ds_read_b128 v[110:113], v110 offset:40960
	v_add_u32_e32 v240, v0, v194
	ds_read_b128 v[240:243], v240 offset:32768
	v_add_u32_e32 v244, v0, v194
	ds_read_b128 v[244:247], v244 offset:40960
	v_add_u32_e32 v248, v0, v193
	ds_read_b128 v[248:251], v248 offset:32768
	s_waitcnt lgkmcnt(8)
	v_mfma_f32_32x32x16_bf16 v[82:97], v[66:69], v[114:117], 0
	s_waitcnt lgkmcnt(7)
	v_mfma_f32_32x32x16_bf16 v[66:81], v[70:73], v[114:117], 0
	s_waitcnt lgkmcnt(6)
	v_mfma_f32_32x32x16_bf16 v[82:97], v[98:101], v[118:121], v[82:97]
	v_add_u32_e32 v98, v0, v193
	ds_read_b128 v[98:101], v98 offset:40960
	s_waitcnt lgkmcnt(6)
	v_mfma_f32_32x32x16_bf16 v[66:81], v[102:105], v[118:121], v[66:81]
	v_add_u32_e32 v102, v0, v192
	ds_read_b128 v[102:105], v102 offset:32768
	s_waitcnt lgkmcnt(6)
	v_mfma_f32_32x32x16_bf16 v[82:97], v[106:109], v[122:125], v[82:97]
	v_add_u32_e32 v106, v0, v192
	ds_read_b128 v[106:109], v106 offset:40960
	s_waitcnt lgkmcnt(6)
	v_mfma_f32_32x32x16_bf16 v[66:81], v[110:113], v[122:125], v[66:81]
	v_add_u32_e32 v110, v0, v191
	ds_read_b128 v[110:113], v110 offset:32768
	s_waitcnt lgkmcnt(6)
	v_mfma_f32_32x32x16_bf16 v[82:97], v[240:243], v[126:129], v[82:97]
	v_add_u32_e32 v240, v0, v191
	ds_read_b128 v[240:243], v240 offset:40960
	s_waitcnt lgkmcnt(6)
	v_mfma_f32_32x32x16_bf16 v[66:81], v[244:247], v[126:129], v[66:81]
	v_add_u32_e32 v244, v0, v190
	ds_read_b128 v[244:247], v244 offset:32768
	s_waitcnt lgkmcnt(6)
	v_mfma_f32_32x32x16_bf16 v[82:97], v[248:251], v[130:133], v[82:97]
	v_add_u32_e32 v248, v0, v190
	ds_read_b128 v[248:251], v248 offset:40960
	s_waitcnt lgkmcnt(6)
	v_mfma_f32_32x32x16_bf16 v[66:81], v[98:101], v[130:133], v[66:81]
	s_waitcnt lgkmcnt(5)
	v_mfma_f32_32x32x16_bf16 v[82:97], v[102:105], v[134:137], v[82:97]
	s_waitcnt lgkmcnt(4)
	v_mfma_f32_32x32x16_bf16 v[66:81], v[106:109], v[134:137], v[66:81]
	s_waitcnt lgkmcnt(3)
	v_mfma_f32_32x32x16_bf16 v[82:97], v[110:113], v[138:141], v[82:97]
	s_waitcnt lgkmcnt(2)
	v_mfma_f32_32x32x16_bf16 v[66:81], v[240:243], v[138:141], v[66:81]
	s_waitcnt lgkmcnt(1)
	v_mfma_f32_32x32x16_bf16 v[82:97], v[244:247], v[142:145], v[82:97]
	s_waitcnt lgkmcnt(0)
	v_mfma_f32_32x32x16_bf16 v[66:81], v[248:251], v[142:145], v[66:81]
	s_add_i32 s72, s2, s92
	v_med3_i32 v239, s72, -7, 7
	v_lshlrev_b32_e32 v239, 7, v239
	v_lshl_add_u32 v239, v183, 2, v239
	v_add_u32_e32 v239, 0x10bbc, v239
	ds_read2_b32 v[206:207], v239 offset0:0 offset1:32
	ds_read2_b32 v[208:209], v239 offset0:1 offset1:33
	ds_read2_b32 v[210:211], v239 offset0:2 offset1:34
	ds_read2_b32 v[212:213], v239 offset0:3 offset1:35
	ds_read2_b32 v[214:215], v239 offset0:8 offset1:40
	ds_read2_b32 v[216:217], v239 offset0:9 offset1:41
	ds_read2_b32 v[218:219], v239 offset0:10 offset1:42
	ds_read2_b32 v[220:221], v239 offset0:11 offset1:43
	ds_read2_b32 v[222:223], v239 offset0:16 offset1:48
	ds_read2_b32 v[224:225], v239 offset0:17 offset1:49
	ds_read2_b32 v[226:227], v239 offset0:18 offset1:50
	ds_read2_b32 v[228:229], v239 offset0:19 offset1:51
	ds_read2_b32 v[230:231], v239 offset0:24 offset1:56
	ds_read2_b32 v[232:233], v239 offset0:25 offset1:57
	ds_read2_b32 v[234:235], v239 offset0:26 offset1:58
	s_waitcnt lgkmcnt(14)
	ds_read2_b32 v[236:237], v239 offset0:27 offset1:59
	v_mov_b32_e32 v238, 0xff800000
	s_nop 11
	s_waitcnt lgkmcnt(0)
	v_readlane_b32 s98, v252, 11
	v_add_f32_e32 v230, v94, v230
	v_cndmask_b32_e64 v94, v238, v230, s[20:21]
	v_add_f32_e32 v232, v95, v232
	v_cndmask_b32_e64 v95, v238, v232, s[16:17]
	v_add_f32_e32 v234, v96, v234
	v_cndmask_b32_e64 v96, v238, v234, s[12:13]
	v_add_f32_e32 v236, v97, v236
	v_cndmask_b32_e64 v97, v238, v236, s[8:9]
	v_add_f32_e32 v207, v66, v207
	v_cndmask_b32_e64 v0, v238, v207, s[68:69]
	v_add_f32_e32 v209, v67, v209
	v_cndmask_b32_e64 v66, v238, v209, s[64:65]
	v_add_f32_e32 v211, v68, v211
	v_cndmask_b32_e64 v67, v238, v211, s[60:61]
	v_add_f32_e32 v213, v69, v213
	v_cndmask_b32_e64 v68, v238, v213, s[56:57]
	s_bitcmp1_b32 s98, 6
	s_cbranch_scc1 .Lna1_odd
	v_add_f32_e32 v206, v82, v206
	v_cndmask_b32_e64 v82, v238, v206, s[70:71]
	v_add_f32_e32 v208, v83, v208
	v_cndmask_b32_e64 v83, v238, v208, s[66:67]
	v_add_f32_e32 v210, v84, v210
	v_cndmask_b32_e64 v84, v238, v210, s[62:63]
	v_add_f32_e32 v212, v85, v212
	v_cndmask_b32_e64 v85, v238, v212, s[58:59]
	v_add_f32_e32 v214, v86, v214
	v_cndmask_b32_e64 v86, v238, v214, s[54:55]
	v_add_f32_e32 v216, v87, v216
	v_cndmask_b32_e64 v87, v238, v216, s[50:51]
	v_add_f32_e32 v218, v88, v218
	v_cndmask_b32_e64 v88, v238, v218, s[46:47]
	v_add_f32_e32 v220, v89, v220
	v_cndmask_b32_e64 v89, v238, v220, s[42:43]
	v_add_f32_e32 v222, v90, v222
	v_cndmask_b32_e64 v90, v238, v222, s[38:39]
	v_add_f32_e32 v224, v91, v224
	v_cndmask_b32_e64 v91, v238, v224, s[34:35]
	v_add_f32_e32 v226, v92, v226
	v_cndmask_b32_e64 v92, v238, v226, s[28:29]
	v_add_f32_e32 v228, v93, v228
	v_cndmask_b32_e64 v93, v238, v228, s[24:25]
	v_max_f32_e32 v81, v94, v95
	v_max3_f32 v81, v81, v96, v97
	v_max3_f32 v81, v81, v0, v66
	v_max3_f32 v81, v81, v67, v68
	v_max3_f32 v81, v81, v82, v83
	v_max3_f32 v81, v81, v84, v85
	v_max3_f32 v81, v81, v86, v87
	v_max3_f32 v81, v81, v88, v89
	v_max3_f32 v81, v81, v90, v91
	v_max3_f32 v81, v81, v92, v93
	s_branch .Lna1_join
.Lna1_odd:
	v_add_f32_e32 v215, v70, v215
	v_cndmask_b32_e64 v69, v238, v215, s[52:53]
	v_add_f32_e32 v217, v71, v217
	v_cndmask_b32_e64 v70, v238, v217, s[48:49]
	v_add_f32_e32 v219, v72, v219
	v_cndmask_b32_e64 v71, v238, v219, s[44:45]
	v_add_f32_e32 v221, v73, v221
	v_cndmask_b32_e64 v72, v238, v221, s[40:41]
	v_add_f32_e32 v223, v74, v223
	v_cndmask_b32_e64 v73, v238, v223, s[36:37]
	v_add_f32_e32 v225, v75, v225
	v_cndmask_b32_e64 v74, v238, v225, s[30:31]
	v_add_f32_e32 v227, v76, v227
	v_cndmask_b32_e64 v75, v238, v227, s[26:27]
	v_add_f32_e32 v229, v77, v229
	v_cndmask_b32_e64 v76, v238, v229, s[22:23]
	v_add_f32_e32 v231, v78, v231
	v_cndmask_b32_e64 v77, v238, v231, s[18:19]
	v_add_f32_e32 v233, v79, v233
	v_cndmask_b32_e64 v78, v238, v233, s[14:15]
	v_add_f32_e32 v235, v80, v235
	v_cndmask_b32_e64 v79, v238, v235, s[10:11]
	v_add_f32_e32 v237, v81, v237
	v_cndmask_b32_e64 v80, v238, v237, s[6:7]
	v_max_f32_e32 v81, v94, v95
	v_max3_f32 v81, v81, v96, v97
	v_max3_f32 v81, v81, v0, v66
	v_max3_f32 v81, v81, v67, v68
	v_max3_f32 v81, v81, v69, v70
	v_max3_f32 v81, v81, v71, v72
	v_max3_f32 v81, v81, v73, v74
	v_max3_f32 v81, v81, v75, v76
	v_max3_f32 v81, v81, v77, v78
	v_max3_f32 v81, v81, v79, v80
.Lna1_join:
	v_mov_b32_e32 v98, v81
	s_nop 1
	v_permlane32_swap_b32_e32 v81, v98
	v_max_f32_e32 v98, v98, v98
	v_max_f32_e32 v81, v81, v81
	v_max_f32_e32 v81, v81, v98
	v_sub_f32_e32 v98, v81, v184
	v_cmp_ge_f32_e32 vcc, s82, v98
	v_max_f32_e32 v98, v184, v184
	v_max_f32_e32 v98, v98, v81
	v_sub_f32_e32 v81, v184, v98
	v_mul_f32_e32 v81, 0x3e0293ee, v81
	v_exp_f32_e32 v81, v81
	s_cmp_eq_u64 vcc, exec
	s_cselect_b64 s[72:73], -1, 0
	v_cndmask_b32_e64 v81, v81, 1.0, s[72:73]
	v_cmp_gt_f32_e32 vcc, 1.0, v81
	s_cbranch_vccz .LBB0_601
	s_and_saveexec_b64 s[86:87], s[4:5]
	ds_write_b32 v179, v81 offset:128
	s_or_b64 exec, exec, s[86:87]
	s_waitcnt lgkmcnt(0)
	v_add_u32_e32 v99, s89, v178
	ds_read_b128 v[100:103], v99 offset:224
	ds_read_b128 v[104:107], v99 offset:192
	ds_read_b128 v[108:111], v99 offset:160
	ds_read_b128 v[202:205], v99 offset:128
	s_waitcnt lgkmcnt(3)
	v_pk_mul_f32 v[62:63], v[62:63], v[100:101]
	s_waitcnt lgkmcnt(2)
	v_pk_mul_f32 v[58:59], v[58:59], v[104:105]
	s_waitcnt lgkmcnt(1)
	v_pk_mul_f32 v[54:55], v[54:55], v[108:109]
	v_pk_mul_f32 v[64:65], v[64:65], v[102:103]
	v_pk_mul_f32 v[60:61], v[60:61], v[106:107]
	v_pk_mul_f32 v[56:57], v[56:57], v[110:111]
	s_waitcnt lgkmcnt(0)
	v_pk_mul_f32 v[52:53], v[52:53], v[204:205]
	v_pk_mul_f32 v[50:51], v[50:51], v[202:203]
	v_pk_mul_f32 v[46:47], v[46:47], v[100:101]
	v_pk_mul_f32 v[42:43], v[42:43], v[104:105]
	v_pk_mul_f32 v[38:39], v[38:39], v[108:109]
	v_pk_mul_f32 v[48:49], v[48:49], v[102:103]
	v_pk_mul_f32 v[44:45], v[44:45], v[106:107]
	v_pk_mul_f32 v[40:41], v[40:41], v[110:111]
	v_pk_mul_f32 v[36:37], v[36:37], v[204:205]
	v_pk_mul_f32 v[34:35], v[34:35], v[202:203]
	v_pk_mul_f32 v[30:31], v[30:31], v[100:101]
	v_pk_mul_f32 v[26:27], v[26:27], v[104:105]
	v_pk_mul_f32 v[22:23], v[22:23], v[108:109]
	v_pk_mul_f32 v[32:33], v[32:33], v[102:103]
	v_pk_mul_f32 v[28:29], v[28:29], v[106:107]
	v_pk_mul_f32 v[24:25], v[24:25], v[110:111]
	v_pk_mul_f32 v[20:21], v[20:21], v[204:205]
	v_pk_mul_f32 v[18:19], v[18:19], v[202:203]
	v_pk_mul_f32 v[14:15], v[14:15], v[100:101]
	v_pk_mul_f32 v[10:11], v[10:11], v[104:105]
	v_pk_mul_f32 v[6:7], v[6:7], v[108:109]
	v_pk_mul_f32 v[16:17], v[16:17], v[102:103]
	v_pk_mul_f32 v[12:13], v[12:13], v[106:107]
	v_pk_mul_f32 v[8:9], v[8:9], v[110:111]
	v_pk_mul_f32 v[4:5], v[4:5], v[204:205]
	v_pk_mul_f32 v[2:3], v[2:3], v[202:203]
.LBB0_601:
	v_cndmask_b32_e64 v184, v98, v184, s[72:73]
	v_mul_f32_e32 v98, 0xbe0293ee, v184
	v_fmamk_f32 v94, v94, 0x3e0293ee, v98
	v_fmamk_f32 v95, v95, 0x3e0293ee, v98
	v_fmamk_f32 v96, v96, 0x3e0293ee, v98
	v_fmamk_f32 v97, v97, 0x3e0293ee, v98
	v_fmamk_f32 v0, v0, 0x3e0293ee, v98
	v_fmamk_f32 v66, v66, 0x3e0293ee, v98
	v_fmamk_f32 v67, v67, 0x3e0293ee, v98
	v_fmamk_f32 v68, v68, 0x3e0293ee, v98
	s_bitcmp1_b32 s98, 6
	s_cbranch_scc1 .Lna2_odd
	v_fmamk_f32 v82, v82, 0x3e0293ee, v98
	v_fmamk_f32 v83, v83, 0x3e0293ee, v98
	v_fmamk_f32 v84, v84, 0x3e0293ee, v98
	v_fmamk_f32 v85, v85, 0x3e0293ee, v98
	v_fmamk_f32 v86, v86, 0x3e0293ee, v98
	v_fmamk_f32 v87, v87, 0x3e0293ee, v98
	v_fmamk_f32 v88, v88, 0x3e0293ee, v98
	v_fmamk_f32 v89, v89, 0x3e0293ee, v98
	v_fmamk_f32 v90, v90, 0x3e0293ee, v98
	v_fmamk_f32 v91, v91, 0x3e0293ee, v98
	v_fmamk_f32 v92, v92, 0x3e0293ee, v98
	v_fmamk_f32 v93, v93, 0x3e0293ee, v98
	v_exp_f32_e32 v80, v82
	v_exp_f32_e32 v82, v83
	v_exp_f32_e32 v83, v84
	v_exp_f32_e32 v84, v85
	v_exp_f32_e32 v85, v86
	v_exp_f32_e32 v86, v87
	v_exp_f32_e32 v87, v88
	v_exp_f32_e32 v88, v89
	v_exp_f32_e32 v89, v90
	v_exp_f32_e32 v90, v91
	v_exp_f32_e32 v91, v92
	v_exp_f32_e32 v92, v93
	v_exp_f32_e32 v93, v94
	v_exp_f32_e32 v94, v95
	v_exp_f32_e32 v95, v96
	v_exp_f32_e32 v96, v97
	v_exp_f32_e32 v97, v0
	v_exp_f32_e32 v99, v66
	v_exp_f32_e32 v100, v67
	v_exp_f32_e32 v101, v68
	v_add_f32_e32 v0, v80, v82
	v_add_f32_e32 v0, v83, v0
	v_add_f32_e32 v0, v84, v0
	v_add_f32_e32 v0, v85, v0
	v_add_f32_e32 v0, v86, v0
	v_add_f32_e32 v0, v87, v0
	v_add_f32_e32 v0, v88, v0
	v_add_f32_e32 v0, v89, v0
	v_add_f32_e32 v0, v90, v0
	v_add_f32_e32 v0, v91, v0
	v_add_f32_e32 v0, v92, v0
	v_add_f32_e32 v0, v93, v0
	v_add_f32_e32 v0, v94, v0
	v_add_f32_e32 v0, v95, v0
	v_add_f32_e32 v0, v96, v0
	v_add_f32_e32 v0, v97, v0
	v_add_f32_e32 v0, v99, v0
	v_add_f32_e32 v0, v100, v0
	v_add_f32_e32 v0, v101, v0
	v_mov_b32_e32 v66, v0
	s_nop 1
	v_permlane32_swap_b32_e32 v0, v66
	v_add_f32_e32 v0, v0, v66
	v_fmac_f32_e32 v0, v200, v81
	v_cvt_pk_bf16_f32 v66, v80, v82
	v_cvt_pk_bf16_f32 v67, v83, v84
	v_cvt_pk_bf16_f32 v68, v85, v86
	v_cvt_pk_bf16_f32 v69, v87, v88
	v_cvt_pk_bf16_f32 v70, v89, v90
	v_cvt_pk_bf16_f32 v71, v91, v92
	v_cvt_pk_bf16_f32 v72, v93, v94
	v_cvt_pk_bf16_f32 v73, v95, v96
	v_cvt_pk_bf16_f32 v74, v97, v99
	v_cvt_pk_bf16_f32 v75, v100, v101
	v_mov_b32_e32 v76, 0
	v_mov_b32_e32 v77, 0
	v_mov_b32_e32 v78, 0
	v_mov_b32_e32 v79, 0
	v_mov_b32_e32 v80, 0
	v_mov_b32_e32 v81, 0
	s_branch .Lna2_join
.Lna2_odd:
	v_fmamk_f32 v69, v69, 0x3e0293ee, v98
	v_fmamk_f32 v70, v70, 0x3e0293ee, v98
	v_fmamk_f32 v71, v71, 0x3e0293ee, v98
	v_fmamk_f32 v72, v72, 0x3e0293ee, v98
	v_fmamk_f32 v73, v73, 0x3e0293ee, v98
	v_fmamk_f32 v74, v74, 0x3e0293ee, v98
	v_fmamk_f32 v75, v75, 0x3e0293ee, v98
	v_fmamk_f32 v76, v76, 0x3e0293ee, v98
	v_fmamk_f32 v77, v77, 0x3e0293ee, v98
	v_fmamk_f32 v78, v78, 0x3e0293ee, v98
	v_fmamk_f32 v79, v79, 0x3e0293ee, v98
	v_fmac_f32_e32 v98, 0x3e0293ee, v80
	v_exp_f32_e32 v93, v94
	v_exp_f32_e32 v94, v95
	v_exp_f32_e32 v95, v96
	v_exp_f32_e32 v96, v97
	v_exp_f32_e32 v97, v0
	v_exp_f32_e32 v99, v66
	v_exp_f32_e32 v100, v67
	v_exp_f32_e32 v101, v68
	v_exp_f32_e32 v102, v69
	v_exp_f32_e32 v103, v70
	v_exp_f32_e32 v104, v71
	v_exp_f32_e32 v105, v72
	v_exp_f32_e32 v106, v73
	v_exp_f32_e32 v107, v74
	v_exp_f32_e32 v108, v75
	v_exp_f32_e32 v109, v76
	v_exp_f32_e32 v110, v77
	v_exp_f32_e32 v111, v78
	v_exp_f32_e32 v112, v79
	v_exp_f32_e32 v98, v98
	v_add_f32_e32 v0, v93, v94
	v_add_f32_e32 v0, v95, v0
	v_add_f32_e32 v0, v96, v0
	v_add_f32_e32 v0, v97, v0
	v_add_f32_e32 v0, v99, v0
	v_add_f32_e32 v0, v100, v0
	v_add_f32_e32 v0, v101, v0
	v_add_f32_e32 v0, v102, v0
	v_add_f32_e32 v0, v103, v0
	v_add_f32_e32 v0, v104, v0
	v_add_f32_e32 v0, v105, v0
	v_add_f32_e32 v0, v106, v0
	v_add_f32_e32 v0, v107, v0
	v_add_f32_e32 v0, v108, v0
	v_add_f32_e32 v0, v109, v0
	v_add_f32_e32 v0, v110, v0
	v_add_f32_e32 v0, v111, v0
	v_add_f32_e32 v0, v112, v0
	v_add_f32_e32 v0, v98, v0
	v_mov_b32_e32 v66, v0
	s_nop 1
	v_permlane32_swap_b32_e32 v0, v66
	v_add_f32_e32 v0, v0, v66
	v_fmac_f32_e32 v0, v200, v81
	v_mov_b32_e32 v66, 0
	v_mov_b32_e32 v67, 0
	v_mov_b32_e32 v68, 0
	v_mov_b32_e32 v69, 0
	v_mov_b32_e32 v70, 0
	v_mov_b32_e32 v71, 0
	v_cvt_pk_bf16_f32 v72, v93, v94
	v_cvt_pk_bf16_f32 v73, v95, v96
	v_cvt_pk_bf16_f32 v74, v97, v99
	v_cvt_pk_bf16_f32 v75, v100, v101
	v_cvt_pk_bf16_f32 v76, v102, v103
	v_cvt_pk_bf16_f32 v77, v104, v105
	v_cvt_pk_bf16_f32 v78, v106, v107
	v_cvt_pk_bf16_f32 v79, v108, v109
	v_cvt_pk_bf16_f32 v80, v110, v111
	v_cvt_pk_bf16_f32 v81, v112, v98
.Lna2_join:
	s_nop 0
	v_permlane32_swap_b32_e32 v66, v68
	v_permlane32_swap_b32_e32 v67, v69
	v_permlane32_swap_b32_e32 v70, v72
	v_permlane32_swap_b32_e32 v71, v73
	v_permlane32_swap_b32_e32 v74, v76
	v_permlane32_swap_b32_e32 v75, v77
	v_permlane32_swap_b32_e32 v78, v80
	v_permlane32_swap_b32_e32 v79, v81
	v_add_u32_e32 v98, s1, v182
	ds_read_b64_tr_b16 v[82:83], v98 offset:0
	ds_read_b64_tr_b16 v[84:85], v98 offset:0x800
	ds_read_b64_tr_b16 v[86:87], v98 offset:0x1000
	ds_read_b64_tr_b16 v[88:89], v98 offset:0x1800
	ds_read_b64_tr_b16 v[90:91], v98 offset:0x2000
	ds_read_b64_tr_b16 v[92:93], v98 offset:0x2800
	ds_read_b64_tr_b16 v[94:95], v98 offset:0x3000
	ds_read_b64_tr_b16 v[96:97], v98 offset:0x3800
	s_waitcnt lgkmcnt(0)
	s_nop 0
	v_mfma_f32_32x32x16_bf16 v[50:65], v[66:69], v[82:85], v[50:65]
	ds_read_b64_tr_b16 v[82:83], v98 offset:0x200
	ds_read_b64_tr_b16 v[84:85], v98 offset:0xa00
	v_mfma_f32_32x32x16_bf16 v[50:65], v[70:73], v[86:89], v[50:65]
	ds_read_b64_tr_b16 v[86:87], v98 offset:0x1200
	ds_read_b64_tr_b16 v[88:89], v98 offset:0x1a00
	v_mfma_f32_32x32x16_bf16 v[50:65], v[74:77], v[90:93], v[50:65]
	ds_read_b64_tr_b16 v[90:91], v98 offset:0x2200
	ds_read_b64_tr_b16 v[92:93], v98 offset:0x2a00
	v_mfma_f32_32x32x16_bf16 v[50:65], v[78:81], v[94:97], v[50:65]
	ds_read_b64_tr_b16 v[94:95], v98 offset:0x3200
	ds_read_b64_tr_b16 v[96:97], v98 offset:0x3a00
	s_waitcnt lgkmcnt(0)
	v_mfma_f32_32x32x16_bf16 v[34:49], v[66:69], v[82:85], v[34:49]
	ds_read_b64_tr_b16 v[82:83], v98 offset:0x400
	ds_read_b64_tr_b16 v[84:85], v98 offset:0xc00
	v_mfma_f32_32x32x16_bf16 v[34:49], v[70:73], v[86:89], v[34:49]
	ds_read_b64_tr_b16 v[86:87], v98 offset:0x1400
	ds_read_b64_tr_b16 v[88:89], v98 offset:0x1c00
	v_mfma_f32_32x32x16_bf16 v[34:49], v[74:77], v[90:93], v[34:49]
	ds_read_b64_tr_b16 v[90:91], v98 offset:0x2400
	ds_read_b64_tr_b16 v[92:93], v98 offset:0x2c00
	v_mfma_f32_32x32x16_bf16 v[34:49], v[78:81], v[94:97], v[34:49]
	ds_read_b64_tr_b16 v[94:95], v98 offset:0x3400
	ds_read_b64_tr_b16 v[96:97], v98 offset:0x3c00
	s_waitcnt lgkmcnt(0)
	v_mfma_f32_32x32x16_bf16 v[18:33], v[66:69], v[82:85], v[18:33]
	ds_read_b64_tr_b16 v[82:83], v98 offset:0x600
	ds_read_b64_tr_b16 v[84:85], v98 offset:0xe00
	v_mfma_f32_32x32x16_bf16 v[18:33], v[70:73], v[86:89], v[18:33]
	ds_read_b64_tr_b16 v[86:87], v98 offset:0x1600
	ds_read_b64_tr_b16 v[88:89], v98 offset:0x1e00
	v_mfma_f32_32x32x16_bf16 v[18:33], v[74:77], v[90:93], v[18:33]
	ds_read_b64_tr_b16 v[90:91], v98 offset:0x2600
	ds_read_b64_tr_b16 v[92:93], v98 offset:0x2e00
	v_mfma_f32_32x32x16_bf16 v[18:33], v[78:81], v[94:97], v[18:33]
	ds_read_b64_tr_b16 v[94:95], v98 offset:0x3600
	ds_read_b64_tr_b16 v[96:97], v98 offset:0x3e00
	s_waitcnt lgkmcnt(0)
	v_mfma_f32_32x32x16_bf16 v[2:17], v[66:69], v[82:85], v[2:17]
	s_waitcnt vmcnt(3)
	v_cvt_f32_fp8_e32 v66, v164
	v_cvt_f32_fp8_sdwa v67, v164 src0_sel:BYTE_1
	s_waitcnt vmcnt(0)
	v_cvt_pk_bf16_f32 v66, v66, v67
	v_cvt_f32_fp8_sdwa v67, v164 src0_sel:BYTE_2
	v_cvt_f32_fp8_sdwa v68, v164 src0_sel:BYTE_3
	v_cvt_pk_bf16_f32 v67, v67, v68
	v_mfma_f32_32x32x16_bf16 v[2:17], v[70:73], v[86:89], v[2:17]
	v_cvt_f32_fp8_e32 v68, v165
	v_cvt_f32_fp8_sdwa v69, v165 src0_sel:BYTE_1
	v_cvt_pk_bf16_f32 v68, v68, v69
	v_cvt_f32_fp8_sdwa v69, v165 src0_sel:BYTE_2
	v_cvt_f32_fp8_sdwa v70, v165 src0_sel:BYTE_3
	v_cvt_pk_bf16_f32 v69, v69, v70
	s_waitcnt vmcnt(2)
	v_cvt_f32_fp8_e32 v70, v162
	v_mfma_f32_32x32x16_bf16 v[2:17], v[74:77], v[90:93], v[2:17]
	v_cvt_f32_fp8_sdwa v71, v162 src0_sel:BYTE_1
	v_cvt_pk_bf16_f32 v70, v70, v71
	v_cvt_f32_fp8_sdwa v71, v162 src0_sel:BYTE_2
	v_cvt_f32_fp8_sdwa v72, v162 src0_sel:BYTE_3
	v_cvt_pk_bf16_f32 v71, v71, v72
	v_cvt_f32_fp8_e32 v72, v163
	v_cvt_f32_fp8_sdwa v73, v163 src0_sel:BYTE_1
	v_cvt_pk_bf16_f32 v72, v72, v73
	v_cvt_f32_fp8_sdwa v73, v163 src0_sel:BYTE_2
	v_cvt_f32_fp8_sdwa v74, v163 src0_sel:BYTE_3
	v_cvt_pk_bf16_f32 v73, v73, v74
	s_waitcnt vmcnt(1)
	v_mfma_f32_32x32x16_bf16 v[2:17], v[78:81], v[94:97], v[2:17]
	s_waitcnt vmcnt(0)
	v_cvt_f32_fp8_e32 v82, v160
	v_cvt_f32_fp8_sdwa v74, v160 src0_sel:BYTE_1
	v_cvt_f32_fp8_sdwa v83, v160 src0_sel:BYTE_2
	v_cvt_f32_fp8_sdwa v75, v160 src0_sel:BYTE_3
	v_mul_f32_e32 v86, v74, v74
	v_mul_f32_e32 v87, v75, v75
	v_cvt_f32_fp8_e32 v84, v161
	v_cvt_f32_fp8_sdwa v76, v161 src0_sel:BYTE_1
	v_fmac_f32_e32 v86, v82, v82
	v_fmac_f32_e32 v87, v83, v83
	v_add_f32_e32 v86, v86, v87
	v_mul_f32_e32 v87, v76, v76
	v_cvt_f32_fp8_sdwa v85, v161 src0_sel:BYTE_2
	v_cvt_f32_fp8_sdwa v77, v161 src0_sel:BYTE_3
	v_fmac_f32_e32 v87, v84, v84
	v_add_f32_e32 v86, v86, v87
	v_mul_f32_e32 v87, v77, v77
	v_fmac_f32_e32 v87, v85, v85
	v_add_f32_e32 v86, v86, v87
	s_nop 1
	s_xor_b32 s1, s1, 0x4000
	s_add_i32 s1, s1, 0
	s_add_i32 s92, s92, 1
	s_addk_i32 s3, 0x4000
	v_add_f32_dpp v86, v86, v86 quad_perm:[1,0,3,2] row_mask:0xf bank_mask:0xf
	s_nop 1
	s_add_u32 s96, s96, 0x2000
	s_addc_u32 s97, s97, 0
	s_cmp_eq_u32 s96, 0x18000
	v_add_f32_dpp v86, v86, v86 quad_perm:[2,3,0,1] row_mask:0xf bank_mask:0xf
	s_nop 1
	v_add_f32_dpp v86, v86, v86 row_half_mirror row_mask:0xf bank_mask:0xf
	s_nop 1
	s_waitcnt lgkmcnt(0)
	v_add_f32_dpp v86, v86, v86 row_mirror row_mask:0xf bank_mask:0xf
	v_fmamk_f32 v86, v86, 0x3c000000, v167
	v_rsq_f32_e32 v86, v86
	s_nop 0
	v_mul_f32_e32 v82, v86, v82
	v_mul_f32_e32 v74, v86, v74
	v_mul_f32_e32 v82, v150, v82
	v_mul_f32_e32 v74, v151, v74
	v_cvt_pk_bf16_f32 v74, v82, v74
	v_mul_f32_e32 v82, v86, v83
	v_mul_f32_e32 v75, v86, v75
	v_mul_f32_e32 v82, v152, v82
	v_mul_f32_e32 v75, v153, v75
	v_cvt_pk_bf16_f32 v75, v82, v75
	v_mul_f32_e32 v82, v86, v84
	v_mul_f32_e32 v76, v86, v76
	v_mul_f32_e32 v82, v146, v82
	v_mul_f32_e32 v76, v147, v76
	v_cvt_pk_bf16_f32 v76, v82, v76
	v_mul_f32_e32 v82, v86, v85
	v_mul_f32_e32 v77, v86, v77
	v_mul_f32_e32 v82, v148, v82
	v_mul_f32_e32 v77, v149, v77
	v_cvt_pk_bf16_f32 v77, v82, v77
	v_cvt_f32_fp8_e32 v82, v158
	v_cvt_f32_fp8_sdwa v78, v158 src0_sel:BYTE_1
	v_cvt_f32_fp8_sdwa v83, v158 src0_sel:BYTE_2
	v_cvt_f32_fp8_sdwa v79, v158 src0_sel:BYTE_3
	v_mul_f32_e32 v86, v78, v78
	v_mul_f32_e32 v87, v79, v79
	v_cvt_f32_fp8_e32 v84, v159
	v_cvt_f32_fp8_sdwa v80, v159 src0_sel:BYTE_1
	v_fmac_f32_e32 v86, v82, v82
	v_fmac_f32_e32 v87, v83, v83
	v_add_f32_e32 v86, v86, v87
	v_mul_f32_e32 v87, v80, v80
	v_cvt_f32_fp8_sdwa v85, v159 src0_sel:BYTE_2
	v_cvt_f32_fp8_sdwa v81, v159 src0_sel:BYTE_3
	v_fmac_f32_e32 v87, v84, v84
	v_add_f32_e32 v86, v86, v87
	v_mul_f32_e32 v87, v81, v81
	v_fmac_f32_e32 v87, v85, v85
	v_add_f32_e32 v86, v86, v87
	s_nop 1
	v_add_f32_dpp v86, v86, v86 quad_perm:[1,0,3,2] row_mask:0xf bank_mask:0xf
	s_nop 1
	v_add_f32_dpp v86, v86, v86 quad_perm:[2,3,0,1] row_mask:0xf bank_mask:0xf
	s_nop 1
	v_add_f32_dpp v86, v86, v86 row_half_mirror row_mask:0xf bank_mask:0xf
	s_nop 1
	s_waitcnt lgkmcnt(0)
	v_add_f32_dpp v86, v86, v86 row_mirror row_mask:0xf bank_mask:0xf
	v_fmamk_f32 v86, v86, 0x3c000000, v167
	v_rsq_f32_e32 v86, v86
	s_nop 0
	v_mul_f32_e32 v82, v86, v82
	v_mul_f32_e32 v78, v86, v78
	v_mul_f32_e32 v82, v150, v82
	v_mul_f32_e32 v78, v151, v78
	v_cvt_pk_bf16_f32 v78, v82, v78
	v_mul_f32_e32 v82, v86, v83
	v_mul_f32_e32 v79, v86, v79
	v_mul_f32_e32 v82, v152, v82
	v_mul_f32_e32 v79, v153, v79
	v_cvt_pk_bf16_f32 v79, v82, v79
	v_mul_f32_e32 v82, v86, v84
	v_mul_f32_e32 v80, v86, v80
	v_mul_f32_e32 v82, v146, v82
	v_mul_f32_e32 v80, v147, v80
	v_cvt_pk_bf16_f32 v80, v82, v80
	v_mul_f32_e32 v82, v86, v85
	v_mul_f32_e32 v81, v86, v81
	v_mul_f32_e32 v82, v148, v82
	v_mul_f32_e32 v81, v149, v81
	v_cvt_pk_bf16_f32 v81, v82, v81
	v_add_u32_e32 v82, s1, v180
	ds_write_b128 v82, v[66:69]
	v_add_u32_e32 v66, s1, v181
	ds_write_b128 v66, v[70:73]
	v_add_u32_e32 v66, s1, v196
	ds_write_b128 v66, v[74:77] offset:32768
	v_add_u32_e32 v66, s1, v198
	ds_write_b128 v66, v[78:81] offset:32768
	s_waitcnt lgkmcnt(0)
	s_barrier
	s_cbranch_scc1 .Lna_done
	v_mov_b32_e32 v200, v0
	s_branch .LBB0_469
